# select v3: per-wave rotated row order so memory-bound pass 1 overlaps issue-bound passes of other waves
# speedup vs baseline: 1.0078x; 1.0078x over previous
.LBB0_1220:
	s_waitcnt lgkmcnt(0)
	s_barrier
	s_cmpk_gt_i32 s3, 0x1fff
	s_cbranch_scc1 .LBB0_1868
	s_add_u32 s46, s30, 0x17100000
	s_addc_u32 s47, s31, 0
	s_add_u32 s48, s30, 0x69b00000
	s_addc_u32 s49, s31, 0
	s_add_u32 s50, s30, 0x6a300000
	s_addc_u32 s51, s31, 0
	s_add_i32 s52, s2, 0
	s_cmpk_eq_i32 s84, 0x100
	s_waitcnt vmcnt(11)
	v_lshlrev_b64 v[2:3], v50, -1
	s_cselect_b64 s[18:19], -1, 0
	s_abs_i32 s54, s35
	v_not_b32_e32 v52, v2
	v_cvt_f32_u32_e32 v2, s54
	s_sub_i32 s2, 0, s54
	v_mov_b32_e32 v59, 0
	v_lshlrev_b32_e32 v54, 4, v50
	v_rcp_iflag_f32_e32 v2, v2
	v_mov_b32_e32 v55, v59
	v_not_b32_e32 v1, v3
	v_lshlrev_b32_e32 v56, 2, v50
	v_mul_f32_e32 v2, 0x4f7ffffe, v2
	v_cvt_u32_f32_e32 v2, v2
	v_mov_b32_e32 v57, v59
	s_mov_b64 s[4:5], 0x17100000
	v_lshlrev_b32_e32 v4, 7, v50
	v_readfirstlane_b32 s6, v2
	s_mul_i32 s2, s2, s6
	s_mul_hi_u32 s2, s6, s2
	s_add_i32 s56, s6, s2
	v_lshl_add_u64 v[2:3], s[30:31], 0, v[54:55]
	s_mov_b64 s[6:7], 0x17101000
	v_lshl_add_u64 v[60:61], v[2:3], 0, s[6:7]
	v_lshl_add_u64 v[2:3], s[30:31], 0, v[56:57]
	v_lshlrev_b32_e32 v53, 5, v50
	v_lshlrev_b32_e32 v5, 6, v50
	v_lshl_add_u64 v[62:63], v[2:3], 0, s[4:5]
	v_add_u32_e32 v2, s52, v56
	s_mov_b32 s12, 0
	s_movk_i32 s53, 0x100
	v_cmp_eq_u32_e64 s[0:1], 0, v50
	v_or_b32_e32 v66, 31, v53
	v_or_b32_e32 v67, 30, v53
	v_or_b32_e32 v68, 29, v53
	v_or_b32_e32 v69, 28, v53
	v_or_b32_e32 v70, 27, v53
	v_or_b32_e32 v71, 26, v53
	v_or_b32_e32 v72, 25, v53
	v_or_b32_e32 v73, 24, v53
	v_or_b32_e32 v74, 23, v53
	v_or_b32_e32 v75, 22, v53
	v_or_b32_e32 v76, 21, v53
	v_or_b32_e32 v77, 20, v53
	v_or_b32_e32 v78, 19, v53
	v_or_b32_e32 v79, 18, v53
	v_or_b32_e32 v80, 17, v53
	v_or_b32_e32 v81, 16, v53
	v_or_b32_e32 v82, 15, v53
	v_or_b32_e32 v83, 14, v53
	v_or_b32_e32 v84, 13, v53
	v_or_b32_e32 v85, 12, v53
	v_or_b32_e32 v86, 11, v53
	v_or_b32_e32 v87, 10, v53
	v_or_b32_e32 v88, 9, v53
	v_or_b32_e32 v89, 8, v53
	v_or_b32_e32 v90, 7, v53
	v_or_b32_e32 v91, 6, v53
	v_or_b32_e32 v92, 5, v53
	v_or_b32_e32 v93, 4, v53
	v_or_b32_e32 v94, 3, v53
	v_or_b32_e32 v95, 2, v53
	v_or_b32_e32 v96, 1, v53
	v_or_b32_e32 v97, 15, v54
	v_or_b32_e32 v98, 14, v54
	v_or_b32_e32 v99, 13, v54
	v_or_b32_e32 v100, 12, v54
	v_or_b32_e32 v101, 11, v54
	v_or_b32_e32 v102, 10, v54
	v_or_b32_e32 v103, 9, v54
	v_or_b32_e32 v104, 8, v54
	v_or_b32_e32 v105, 7, v54
	v_or_b32_e32 v106, 6, v54
	v_or_b32_e32 v107, 5, v54
	v_or_b32_e32 v108, 4, v54
	v_or_b32_e32 v109, 3, v54
	v_or_b32_e32 v110, 2, v54
	v_or_b32_e32 v111, 1, v54
	v_or_b32_e32 v112, 64, v50
	v_or_b32_e32 v113, 0x80, v50
	v_or_b32_e32 v114, 0xc0, v50
	s_ashr_i32 s55, s35, 31
	v_add_u32_e32 v55, 0x2000, v2
	s_movk_i32 s57, 0xff
	v_mov_b32_e32 v57, 1
	s_mov_b64 s[20:21], 0x1000
	s_mov_b64 s[22:23], 0x100
	v_add_u32_e32 v115, s52, v5
	v_lshlrev_b32_e32 v116, 2, v50
	v_add_u32_e32 v117, s52, v4
	s_cmpk_eq_i32 s84, 0x100
	s_cbranch_scc0 .LBB0_1223
	s_and_b32 s4, s3, 7
	s_lshr_b32 s5, s4, 2
	s_lshl_b32 s5, s5, 1
	s_add_i32 s4, s4, s5
	s_and_b32 s4, s4, 3
	s_lshl_b32 s4, s4, 11
	s_add_i32 s3, s3, s4
	s_and_b32 s3, s3, 0x1fff
	s_mov_b32 s99, 4
	s_branch .LBB0_1223
.LBB0_1222:
	s_cmpk_eq_i32 s84, 0x100
	s_cbranch_scc0 .Lsel_latch_plain
	s_add_i32 s3, s3, s35
	s_and_b32 s3, s3, 0x1fff
	s_add_i32 s99, s99, -1
	s_cmp_lg_u32 s99, 0
	s_cbranch_scc1 .LBB0_1223
	s_branch .LBB0_1867
